# grid barrier leader: XGEN relay atomic issued before the leader CU's own buffer_inv (independent ops; lets the XCD's pollers leave earlier); on top of m15
# speedup vs baseline: 1.0056x; 1.0056x over previous
; DI unsigned xb_ld(unsigned* p)              { return __hip_atomic_load(p, __ATOMIC_RELAXED, __HIP_MEMORY_SCOPE_AGENT); }
; DI unsigned xb_add(unsigned* p, unsigned v) { return __hip_atomic_fetch_add(p, v, __ATOMIC_RELAXED, __HIP_MEMORY_SCOPE_AGENT); }
; #define XB_SPIN(cond, bar) do { unsigned _sp = 0; while (cond) { __builtin_amdgcn_s_sleep(1); \
;     if ((++_sp & 255u) == 0u) { if (xb_ld(&(bar)[XB_TMO])) break; if (_sp > XB_SPIN_CAP) { atomicAdd(&(bar)[XB_TMO], 1u); break; } } } } while (0)
; DI void xcd_barrier(const XcdBarrier& b) {
;     ...
;             const unsigned og = xb_add(&bar[XB_TOP], 1u);
;             const unsigned tg = og / nx;
;             if (og + 1u == (tg + 1u) * nx) xb_add(&bar[XB_TOPGEN], 1u);
;             else XB_SPIN(xb_ld(&bar[XB_TOPGEN]) == tg, bar);
;             __builtin_amdgcn_fence(__ATOMIC_ACQUIRE, "agent");
;             xb_add(&bar[XB_XGEN(b.x)], 1u);
;             asm volatile("s_waitcnt vmcnt(0)" ::: "memory");
.LBB0_258:
	s_or_b64 exec, exec, s[30:31]
	v_readlane_b32 s4, v254, 12
	v_readlane_b32 s5, v254, 13
	v_mov_b32_e32 v1, 1
	s_waitcnt vmcnt(0) lgkmcnt(0)
	v_mov_b64_e32 v[2:3], s[4:5]
	flat_atomic_add v[2:3], v1
	buffer_inv sc1
	s_waitcnt vmcnt(0)

; DI unsigned xb_ld(unsigned* p)              { return __hip_atomic_load(p, __ATOMIC_RELAXED, __HIP_MEMORY_SCOPE_AGENT); }
; DI unsigned xb_add(unsigned* p, unsigned v) { return __hip_atomic_fetch_add(p, v, __ATOMIC_RELAXED, __HIP_MEMORY_SCOPE_AGENT); }
; #define XB_SPIN(cond, bar) do { unsigned _sp = 0; while (cond) { __builtin_amdgcn_s_sleep(1); \
;     if ((++_sp & 255u) == 0u) { if (xb_ld(&(bar)[XB_TMO])) break; if (_sp > XB_SPIN_CAP) { atomicAdd(&(bar)[XB_TMO], 1u); break; } } } } while (0)
; DI void xcd_barrier(const XcdBarrier& b) {
;     ...
;             const unsigned og = xb_add(&bar[XB_TOP], 1u);
;             const unsigned tg = og / nx;
;             if (og + 1u == (tg + 1u) * nx) xb_add(&bar[XB_TOPGEN], 1u);
;             else XB_SPIN(xb_ld(&bar[XB_TOPGEN]) == tg, bar);
;             __builtin_amdgcn_fence(__ATOMIC_ACQUIRE, "agent");
;             xb_add(&bar[XB_XGEN(b.x)], 1u);
;             asm volatile("s_waitcnt vmcnt(0)" ::: "memory");
.LBB0_261:
	s_or_b64 exec, exec, s[16:17]
	v_readlane_b32 s4, v254, 12
	v_readlane_b32 s5, v254, 13
	v_mov_b32_e32 v1, 1
	s_waitcnt vmcnt(0) lgkmcnt(0)
	v_mov_b64_e32 v[2:3], s[4:5]
	flat_atomic_add v[2:3], v1
	buffer_inv sc1
	s_waitcnt vmcnt(0)

; DI unsigned xb_ld(unsigned* p)              { return __hip_atomic_load(p, __ATOMIC_RELAXED, __HIP_MEMORY_SCOPE_AGENT); }
; DI unsigned xb_add(unsigned* p, unsigned v) { return __hip_atomic_fetch_add(p, v, __ATOMIC_RELAXED, __HIP_MEMORY_SCOPE_AGENT); }
; #define XB_SPIN(cond, bar) do { unsigned _sp = 0; while (cond) { __builtin_amdgcn_s_sleep(1); \
;     if ((++_sp & 255u) == 0u) { if (xb_ld(&(bar)[XB_TMO])) break; if (_sp > XB_SPIN_CAP) { atomicAdd(&(bar)[XB_TMO], 1u); break; } } } } while (0)
; DI void xcd_barrier(const XcdBarrier& b) {
;     ...
;             const unsigned og = xb_add(&bar[XB_TOP], 1u);
;             const unsigned tg = og / nx;
;             if (og + 1u == (tg + 1u) * nx) xb_add(&bar[XB_TOPGEN], 1u);
;             else XB_SPIN(xb_ld(&bar[XB_TOPGEN]) == tg, bar);
;             __builtin_amdgcn_fence(__ATOMIC_ACQUIRE, "agent");
;             xb_add(&bar[XB_XGEN(b.x)], 1u);
;             asm volatile("s_waitcnt vmcnt(0)" ::: "memory");
.LBB0_558:
	s_or_b64 exec, exec, s[30:31]
	v_readlane_b32 s6, v254, 12
	v_readlane_b32 s7, v254, 13
	v_mov_b32_e32 v1, 1
	s_waitcnt vmcnt(0) lgkmcnt(0)
	v_mov_b64_e32 v[2:3], s[6:7]
	flat_atomic_add v[2:3], v1
	buffer_inv sc1
	s_waitcnt vmcnt(0)
